# v78 + near-tie blocks out of line + aligned phase entries
# baseline (speedup 1.0000x reference)
.Lg_alldone:
.Lg_nocopy:
	v_mov_b32_e32 v97, 1
	v_cmp_eq_u32_e64 s[2:3], 0, v1
	.p2align 6
.LBB0_118:
	s_waitcnt vmcnt(0)
	v_lshrrev_b32_e32 v67, 4, v0
	v_mov_b32_e32 v66, 0x11100
	v_lshl_or_b32 v66, v67, 2, v66
	s_waitcnt lgkmcnt(0)
	s_barrier
	ds_read_b32 v77, v66 offset:320
	v_mul_u32_u24_e32 v68, 0x102, v67
	v_lshlrev_b32_e32 v72, 3, v68
	v_lshl_add_u32 v68, v138, 3, v72
	v_add_u32_e32 v76, 0x8000, v68
	ds_read2_b64 v[68:71], v76 offset1:16
	v_mul_i32_i24_e32 v73, 0xfffffbf8, v67
	v_lshlrev_b32_e32 v66, 2, v138
	v_add3_u32 v78, v72, v73, v66
	ds_read2_b64 v[72:75], v76 offset0:32 offset1:48
	s_waitcnt lgkmcnt(1)
	v_cvt_f32_f64_e32 v68, v[68:69]
	v_cvt_f32_f64_e32 v69, v[70:71]
	v_mul_f32_e32 v68, v77, v68
	v_mul_f32_e32 v69, v77, v69
	v_fma_f32 v79, v68, v68, 0
	ds_write2_b32 v78, v68, v69 offset1:16
	s_waitcnt lgkmcnt(1)
	v_cvt_f32_f64_e32 v68, v[72:73]
	v_fmac_f32_e32 v79, v69, v69
	v_mul_f32_e32 v72, v77, v68
	ds_read2_b64 v[68:71], v76 offset0:64 offset1:80
	v_cvt_f32_f64_e32 v73, v[74:75]
	v_fmac_f32_e32 v79, v72, v72
	v_mul_f32_e32 v73, v77, v73
	v_fmac_f32_e32 v79, v73, v73
	ds_write2_b32 v78, v72, v73 offset0:32 offset1:48
	ds_read2_b64 v[72:75], v76 offset0:96 offset1:112
	s_waitcnt lgkmcnt(2)
	v_cvt_f32_f64_e32 v68, v[68:69]
	v_cvt_f32_f64_e32 v69, v[70:71]
	v_mul_f32_e32 v68, v77, v68
	v_mul_f32_e32 v69, v77, v69
	v_fmac_f32_e32 v79, v68, v68
	ds_write2_b32 v78, v68, v69 offset0:64 offset1:80
	s_waitcnt lgkmcnt(1)
	v_cvt_f32_f64_e32 v68, v[72:73]
	v_fmac_f32_e32 v79, v69, v69
	v_mul_f32_e32 v72, v77, v68
	ds_read2_b64 v[68:71], v76 offset0:128 offset1:144
	v_cvt_f32_f64_e32 v73, v[74:75]
	v_fmac_f32_e32 v79, v72, v72
	v_mul_f32_e32 v73, v77, v73
	v_fmac_f32_e32 v79, v73, v73
	ds_write2_b32 v78, v72, v73 offset0:96 offset1:112
	ds_read2_b64 v[72:75], v76 offset0:160 offset1:176
	s_waitcnt lgkmcnt(2)
	v_cvt_f32_f64_e32 v68, v[68:69]
	v_cvt_f32_f64_e32 v69, v[70:71]
	v_mul_f32_e32 v68, v77, v68
	v_mul_f32_e32 v69, v77, v69
	v_fmac_f32_e32 v79, v68, v68
	ds_write2_b32 v78, v68, v69 offset0:128 offset1:144
	s_waitcnt lgkmcnt(1)
	v_cvt_f32_f64_e32 v68, v[72:73]
	v_fmac_f32_e32 v79, v69, v69
	v_mul_f32_e32 v72, v77, v68
	ds_read2_b64 v[68:71], v76 offset0:192 offset1:208
	v_cvt_f32_f64_e32 v73, v[74:75]
	v_fmac_f32_e32 v79, v72, v72
	v_mul_f32_e32 v73, v77, v73
	v_fmac_f32_e32 v79, v73, v73
	ds_write2_b32 v78, v72, v73 offset0:160 offset1:176
	ds_read2_b64 v[72:75], v76 offset0:224 offset1:240
	s_waitcnt lgkmcnt(2)
	v_cvt_f32_f64_e32 v68, v[68:69]
	v_cvt_f32_f64_e32 v69, v[70:71]
	v_mul_f32_e32 v68, v77, v68
	v_mul_f32_e32 v69, v77, v69
	v_fmac_f32_e32 v79, v68, v68
	ds_write2_b32 v78, v68, v69 offset0:192 offset1:208
	s_waitcnt lgkmcnt(1)
	v_cvt_f32_f64_e32 v68, v[72:73]
	v_fmac_f32_e32 v79, v69, v69
	v_mul_f32_e32 v68, v77, v68
	v_cvt_f32_f64_e32 v69, v[74:75]
	v_fmac_f32_e32 v79, v68, v68
	v_mul_f32_e32 v69, v77, v69
	v_fmac_f32_e32 v79, v69, v69
	ds_write2_b32 v78, v68, v69 offset0:224 offset1:240
	v_cmp_eq_u32_e32 vcc, 0, v138
	v_add_f32_dpp v68, v79, v79 quad_perm:[1,0,3,2] row_mask:0xf bank_mask:0xf bound_ctrl:1
	s_nop 1
	v_add_f32_dpp v68, v68, v68 quad_perm:[2,3,0,1] row_mask:0xf bank_mask:0xf bound_ctrl:1
	s_nop 1
	v_add_f32_dpp v68, v68, v68 row_half_mirror row_mask:0xf bank_mask:0xf bound_ctrl:1
	s_nop 1
	v_mov_b32_dpp v69, v68 row_mirror row_mask:0xf bank_mask:0xf bound_ctrl:1
	s_and_saveexec_b64 s[0:1], vcc
	v_mov_b32_e32 v70, 0x11200
	v_lshl_or_b32 v67, v67, 2, v70
	v_add_f32_e32 v68, v68, v69
	ds_write_b32 v67, v68
	s_or_b64 exec, exec, s[0:1]
	v_lshlrev_b32_e32 v67, 2, v140
	s_movk_i32 s0, 0x408
	v_mad_u32_u24 v67, v138, s0, v67
	s_waitcnt lgkmcnt(0)
	s_barrier
	ds_read2_b32 v[68:69], v67 offset1:4
	ds_read2_b32 v[70:71], v67 offset0:64 offset1:68
	ds_read2_b32 v[72:73], v67 offset0:192 offset1:196
	s_lshl_b32 s29, s17, 2
	s_lshl_b32 s0, s24, 2
	s_waitcnt lgkmcnt(2)
	v_mfma_f32_16x16x4_f32 a[0:3], v68, v62, 0
	s_add_i32 s0, s0, 0x10100
	s_waitcnt lgkmcnt(1)
	v_mfma_f32_16x16x4_f32 a[4:7], v70, v63, 0
	ds_read2_b32 v[62:63], v67 offset0:128 offset1:132
	s_waitcnt lgkmcnt(0)
	v_mfma_f32_16x16x4_f32 a[0:3], v62, v64, a[0:3]
	v_mfma_f32_16x16x4_f32 a[4:7], v72, v65, a[4:7]
	v_mfma_f32_16x16x4_f32 a[0:3], v69, v58, a[0:3]
	v_mfma_f32_16x16x4_f32 a[4:7], v71, v59, a[4:7]
	ds_read2_b32 v[58:59], v67 offset0:8 offset1:12
	v_mfma_f32_16x16x4_f32 a[0:3], v63, v60, a[0:3]
	ds_read2_b32 v[62:63], v67 offset0:200 offset1:204
	v_mfma_f32_16x16x4_f32 a[4:7], v73, v61, a[4:7]
	ds_read2_b32 v[60:61], v67 offset0:72 offset1:76
	s_waitcnt lgkmcnt(2)
	v_mfma_f32_16x16x4_f32 a[0:3], v58, v54, a[0:3]
	s_waitcnt lgkmcnt(0)
	v_mfma_f32_16x16x4_f32 a[4:7], v60, v55, a[4:7]
	ds_read2_b32 v[54:55], v67 offset0:136 offset1:140
	s_waitcnt lgkmcnt(0)
	v_mfma_f32_16x16x4_f32 a[0:3], v54, v56, a[0:3]
	v_mfma_f32_16x16x4_f32 a[4:7], v62, v57, a[4:7]
	v_mfma_f32_16x16x4_f32 a[0:3], v59, v50, a[0:3]
	v_mfma_f32_16x16x4_f32 a[4:7], v61, v51, a[4:7]
	ds_read2_b32 v[50:51], v67 offset0:16 offset1:20
	v_mfma_f32_16x16x4_f32 a[0:3], v55, v52, a[0:3]
	ds_read2_b32 v[54:55], v67 offset0:208 offset1:212
	v_mfma_f32_16x16x4_f32 a[4:7], v63, v53, a[4:7]
	ds_read2_b32 v[52:53], v67 offset0:80 offset1:84
	s_waitcnt lgkmcnt(2)
	v_mfma_f32_16x16x4_f32 a[0:3], v50, v46, a[0:3]
	s_waitcnt lgkmcnt(0)
	v_mfma_f32_16x16x4_f32 a[4:7], v52, v47, a[4:7]
	ds_read2_b32 v[46:47], v67 offset0:144 offset1:148
	s_waitcnt lgkmcnt(0)
	v_mfma_f32_16x16x4_f32 a[0:3], v46, v48, a[0:3]
	v_mfma_f32_16x16x4_f32 a[4:7], v54, v49, a[4:7]
	v_mfma_f32_16x16x4_f32 a[0:3], v51, v42, a[0:3]
	v_mfma_f32_16x16x4_f32 a[4:7], v53, v43, a[4:7]
	ds_read2_b32 v[42:43], v67 offset0:24 offset1:28
	v_mfma_f32_16x16x4_f32 a[0:3], v47, v44, a[0:3]
	ds_read2_b32 v[46:47], v67 offset0:216 offset1:220
	v_mfma_f32_16x16x4_f32 a[4:7], v55, v45, a[4:7]
	ds_read2_b32 v[44:45], v67 offset0:88 offset1:92
	s_waitcnt lgkmcnt(2)
	v_mfma_f32_16x16x4_f32 a[0:3], v42, v38, a[0:3]
	s_waitcnt lgkmcnt(0)
	v_mfma_f32_16x16x4_f32 a[4:7], v44, v39, a[4:7]
	ds_read2_b32 v[38:39], v67 offset0:152 offset1:156
	s_waitcnt lgkmcnt(0)
	v_mfma_f32_16x16x4_f32 a[0:3], v38, v40, a[0:3]
	v_mfma_f32_16x16x4_f32 a[4:7], v46, v41, a[4:7]
	v_mfma_f32_16x16x4_f32 a[0:3], v43, v34, a[0:3]
	v_mfma_f32_16x16x4_f32 a[4:7], v45, v35, a[4:7]
	ds_read2_b32 v[34:35], v67 offset0:32 offset1:36
	v_mfma_f32_16x16x4_f32 a[0:3], v39, v36, a[0:3]
	ds_read2_b32 v[38:39], v67 offset0:224 offset1:228
	v_mfma_f32_16x16x4_f32 a[4:7], v47, v37, a[4:7]
	ds_read2_b32 v[36:37], v67 offset0:96 offset1:100
	s_waitcnt lgkmcnt(2)
	v_mfma_f32_16x16x4_f32 a[0:3], v34, v30, a[0:3]
	s_waitcnt lgkmcnt(0)
	v_mfma_f32_16x16x4_f32 a[4:7], v36, v31, a[4:7]
	ds_read2_b32 v[30:31], v67 offset0:160 offset1:164
	s_waitcnt lgkmcnt(0)
	v_mfma_f32_16x16x4_f32 a[0:3], v30, v32, a[0:3]
	v_mfma_f32_16x16x4_f32 a[4:7], v38, v33, a[4:7]
	v_mfma_f32_16x16x4_f32 a[0:3], v35, v26, a[0:3]
	v_mfma_f32_16x16x4_f32 a[4:7], v37, v27, a[4:7]
	ds_read2_b32 v[26:27], v67 offset0:40 offset1:44
	v_mfma_f32_16x16x4_f32 a[0:3], v31, v28, a[0:3]
	ds_read2_b32 v[30:31], v67 offset0:232 offset1:236
	v_mfma_f32_16x16x4_f32 a[4:7], v39, v29, a[4:7]
	ds_read2_b32 v[28:29], v67 offset0:104 offset1:108
	s_waitcnt lgkmcnt(2)
	v_mfma_f32_16x16x4_f32 a[0:3], v26, v22, a[0:3]
	s_waitcnt lgkmcnt(0)
	v_mfma_f32_16x16x4_f32 a[4:7], v28, v23, a[4:7]
	ds_read2_b32 v[22:23], v67 offset0:168 offset1:172
	s_waitcnt lgkmcnt(0)
	v_mfma_f32_16x16x4_f32 a[0:3], v22, v24, a[0:3]
	v_mfma_f32_16x16x4_f32 a[4:7], v30, v25, a[4:7]
	v_mfma_f32_16x16x4_f32 a[0:3], v27, v18, a[0:3]
	v_mfma_f32_16x16x4_f32 a[4:7], v29, v19, a[4:7]
	ds_read2_b32 v[18:19], v67 offset0:48 offset1:52
	v_mfma_f32_16x16x4_f32 a[0:3], v23, v20, a[0:3]
	ds_read2_b32 v[22:23], v67 offset0:240 offset1:244
	v_mfma_f32_16x16x4_f32 a[4:7], v31, v21, a[4:7]
	ds_read2_b32 v[20:21], v67 offset0:112 offset1:116
	s_waitcnt lgkmcnt(2)
	v_mfma_f32_16x16x4_f32 a[0:3], v18, v14, a[0:3]
	s_waitcnt lgkmcnt(0)
	v_mfma_f32_16x16x4_f32 a[4:7], v20, v15, a[4:7]
	ds_read2_b32 v[14:15], v67 offset0:176 offset1:180
	s_waitcnt lgkmcnt(0)
	v_mfma_f32_16x16x4_f32 a[0:3], v14, v16, a[0:3]
	v_mfma_f32_16x16x4_f32 a[4:7], v22, v17, a[4:7]
	v_mfma_f32_16x16x4_f32 a[0:3], v19, v10, a[0:3]
	v_mfma_f32_16x16x4_f32 a[4:7], v21, v11, a[4:7]
	ds_read2_b32 v[10:11], v67 offset0:56 offset1:60
	v_mfma_f32_16x16x4_f32 a[0:3], v15, v12, a[0:3]
	ds_read2_b32 v[14:15], v67 offset0:248 offset1:252
	v_mfma_f32_16x16x4_f32 a[4:7], v23, v13, a[4:7]
	ds_read2_b32 v[12:13], v67 offset0:120 offset1:124
	s_waitcnt lgkmcnt(2)
	v_mfma_f32_16x16x4_f32 a[0:3], v10, v6, a[0:3]
	s_waitcnt lgkmcnt(0)
	v_mfma_f32_16x16x4_f32 a[4:7], v12, v7, a[4:7]
	ds_read2_b32 v[6:7], v67 offset0:184 offset1:188
	s_waitcnt lgkmcnt(0)
	v_mfma_f32_16x16x4_f32 a[0:3], v6, v8, a[0:3]
	v_mfma_f32_16x16x4_f32 a[4:7], v14, v9, a[4:7]
	v_mfma_f32_16x16x4_f32 a[0:3], v11, v2, a[0:3]
	v_mov_b32_e32 v2, 0x11300
	v_lshl_add_u32 v2, v134, 2, v2
	ds_read_b32 v2, v2
	v_mfma_f32_16x16x4_f32 a[4:7], v13, v3, a[4:7]
	v_lshlrev_b32_e32 v3, 10, v140
	v_add3_u32 v3, s0, v66, v3
	v_mfma_f32_16x16x4_f32 a[0:3], v7, v4, a[0:3]
	v_or_b32_e32 v7, s29, v140
	v_lshl_or_b32 v4, v7, 8, v66
	v_add_u32_e32 v4, 0x10100, v4
	v_mfma_f32_16x16x4_f32 a[4:7], v15, v5, a[4:7]
	s_nop 9
	v_accvgpr_read_b32 v5, a0
	v_accvgpr_read_b32 v6, a1
	v_accvgpr_read_b32 v8, a2
	v_accvgpr_read_b32 v9, a3
	v_accvgpr_read_b32 v70, a4
	v_accvgpr_read_b32 v71, a5
	v_accvgpr_read_b32 v72, a6
	v_accvgpr_read_b32 v73, a7
	v_add_f32_e32 v5, v5, v70
	v_add_f32_e32 v6, v6, v71
	v_add_f32_e32 v8, v8, v72
	v_add_f32_e32 v9, v9, v73
	s_waitcnt lgkmcnt(0)
	v_fma_f32 v5, -2.0, v5, v2
	v_fma_f32 v6, -2.0, v6, v2
	v_fma_f32 v8, -2.0, v8, v2
	v_fmac_f32_e32 v2, -2.0, v9
	ds_write2st64_b32 v3, v5, v6 offset1:1
	ds_write2st64_b32 v3, v8, v2 offset0:2 offset1:3
	s_waitcnt lgkmcnt(0)
	s_barrier
	ds_read2_b32 v[2:3], v4 offset1:16
	ds_read2_b32 v[4:5], v4 offset0:32 offset1:48
	v_or_b32_e32 v6, 16, v138
	v_or_b32_e32 v8, 32, v138
	v_or_b32_e32 v9, 48, v138
	s_waitcnt lgkmcnt(1)
	v_cmp_lt_f32_e32 vcc, v3, v2
	s_nop 1
	v_cndmask_b32_e32 v10, v2, v3, vcc
	v_cndmask_b32_e32 v6, v138, v6, vcc
	s_waitcnt lgkmcnt(0)
	v_cmp_lt_f32_e32 vcc, v4, v10
	s_nop 1
	v_cndmask_b32_e32 v10, v10, v4, vcc
	v_cndmask_b32_e32 v8, v6, v8, vcc
	v_cmp_lt_f32_e32 vcc, v5, v10
	s_nop 1
	v_cndmask_b32_e32 v6, v10, v5, vcc
	v_cndmask_b32_e32 v14, v8, v9, vcc
	s_nop 0
	v_mov_b32_dpp v9, v6 quad_perm:[1,0,3,2] row_mask:0xf bank_mask:0xf bound_ctrl:1
	v_mov_b32_dpp v8, v14 quad_perm:[1,0,3,2] row_mask:0xf bank_mask:0xf bound_ctrl:1
	v_cmp_gt_f32_e64 s[4:5], v6, v9
	v_cmp_ngt_f32_e32 vcc, v6, v9
	s_and_saveexec_b64 s[6:7], vcc
	v_cmp_eq_f32_e32 vcc, v6, v9
	v_cmp_lt_i32_e64 s[0:1], v8, v14
	s_and_b64 s[0:1], vcc, s[0:1]
	s_andn2_b64 s[4:5], s[4:5], exec
	s_and_b64 s[0:1], s[0:1], exec
	s_or_b64 s[4:5], s[4:5], s[0:1]
	s_or_b64 exec, exec, s[6:7]
	s_and_saveexec_b64 s[0:1], s[4:5]
	v_mov_b32_e32 v6, v9
	v_mov_b32_e32 v14, v8
	s_or_b64 exec, exec, s[0:1]
	v_mov_b32_dpp v9, v6 quad_perm:[2,3,0,1] row_mask:0xf bank_mask:0xf bound_ctrl:1
	v_mov_b32_dpp v8, v14 quad_perm:[2,3,0,1] row_mask:0xf bank_mask:0xf bound_ctrl:1
	v_cmp_gt_f32_e64 s[4:5], v6, v9
	v_cmp_ngt_f32_e32 vcc, v6, v9
	s_and_saveexec_b64 s[6:7], vcc
	v_cmp_eq_f32_e32 vcc, v6, v9
	v_cmp_lt_i32_e64 s[0:1], v8, v14
	s_and_b64 s[0:1], vcc, s[0:1]
	s_andn2_b64 s[4:5], s[4:5], exec
	s_and_b64 s[0:1], s[0:1], exec
	s_or_b64 s[4:5], s[4:5], s[0:1]
	s_or_b64 exec, exec, s[6:7]
	s_and_saveexec_b64 s[0:1], s[4:5]
	v_mov_b32_e32 v6, v9
	v_mov_b32_e32 v14, v8
	s_or_b64 exec, exec, s[0:1]
	v_mov_b32_dpp v9, v6 row_half_mirror row_mask:0xf bank_mask:0xf bound_ctrl:1
	v_mov_b32_dpp v8, v14 row_half_mirror row_mask:0xf bank_mask:0xf bound_ctrl:1
	v_cmp_gt_f32_e64 s[4:5], v6, v9
	v_cmp_ngt_f32_e32 vcc, v6, v9
	s_and_saveexec_b64 s[6:7], vcc
	v_cmp_eq_f32_e32 vcc, v6, v9
	v_cmp_lt_i32_e64 s[0:1], v8, v14
	s_and_b64 s[0:1], vcc, s[0:1]
	s_andn2_b64 s[4:5], s[4:5], exec
	s_and_b64 s[0:1], s[0:1], exec
	s_or_b64 s[4:5], s[4:5], s[0:1]
	s_or_b64 exec, exec, s[6:7]
	s_and_saveexec_b64 s[0:1], s[4:5]
	v_mov_b32_e32 v6, v9
	v_mov_b32_e32 v14, v8
	s_or_b64 exec, exec, s[0:1]
	v_mov_b32_dpp v8, v6 row_mirror row_mask:0xf bank_mask:0xf bound_ctrl:1
	v_mov_b32_dpp v9, v14 row_mirror row_mask:0xf bank_mask:0xf bound_ctrl:1
	v_cmp_gt_f32_e64 s[4:5], v6, v8
	v_cmp_ngt_f32_e32 vcc, v6, v8
	s_and_saveexec_b64 s[6:7], vcc
	v_cmp_eq_f32_e32 vcc, v6, v8
	v_cmp_lt_i32_e64 s[0:1], v9, v14
	s_and_b64 s[0:1], vcc, s[0:1]
	s_andn2_b64 s[4:5], s[4:5], exec
	s_and_b64 s[0:1], s[0:1], exec
	s_or_b64 s[4:5], s[4:5], s[0:1]
	s_or_b64 exec, exec, s[6:7]
	s_and_saveexec_b64 s[0:1], s[4:5]
	v_mov_b32_e32 v6, v8
	v_mov_b32_e32 v14, v9
	s_or_b64 exec, exec, s[0:1]
	v_mov_b32_e32 v8, 0x11280
	ds_read_b32 v8, v8
	v_mov_b32_e32 v9, 0x11200
	v_lshl_add_u32 v7, v7, 2, v9
	ds_read_b32 v9, v7
	v_mov_b32_e32 v13, 0x260
	v_lshlrev_b32_e32 v18, 2, v139
	v_mov_b32_e32 v19, 0
	s_mov_b32 s25, 0
	s_mov_b32 s26, s25
	s_mov_b32 s0, 0x3f800347
	s_mov_b32 s1, 0x3f8020c5
	s_waitcnt lgkmcnt(0)
	v_pk_mul_f32 v[8:9], v[8:9], s[0:1]
	s_mov_b32 s4, 0xf800000
	v_mul_f32_e32 v7, 0x4f800000, v9
	v_cmp_gt_f32_e32 vcc, s4, v9
	s_nop 1
	v_cndmask_b32_e32 v7, v9, v7, vcc
	v_sqrt_f32_e32 v10, v7
	s_nop 0
	v_add_u32_e32 v11, -1, v10
	v_fma_f32 v12, -v11, v10, v7
	v_cmp_ge_f32_e64 s[0:1], 0, v12
	v_add_u32_e32 v12, 1, v10
	s_nop 0
	v_cndmask_b32_e64 v11, v10, v11, s[0:1]
	v_fma_f32 v10, -v12, v10, v7
	v_cmp_lt_f32_e64 s[0:1], 0, v10
	s_nop 1
	v_cndmask_b32_e64 v10, v11, v12, s[0:1]
	v_mul_f32_e32 v11, 0x37800000, v10
	v_cndmask_b32_e32 v10, v10, v11, vcc
	v_mul_f32_e32 v11, 0x4f800000, v8
	v_cmp_gt_f32_e32 vcc, s4, v8
	v_cmp_class_f32_e64 s[0:1], v7, v13
	s_nop 0
	v_cndmask_b32_e32 v11, v8, v11, vcc
	v_sqrt_f32_e32 v12, v11
	v_cndmask_b32_e64 v7, v10, v7, s[0:1]
	v_add_u32_e32 v10, -1, v12
	v_fma_f32 v15, -v10, v12, v11
	v_cmp_ge_f32_e64 s[0:1], 0, v15
	v_add_u32_e32 v15, 1, v12
	s_nop 0
	v_cndmask_b32_e64 v10, v12, v10, s[0:1]
	v_fma_f32 v12, -v15, v12, v11
	v_cmp_lt_f32_e64 s[0:1], 0, v12
	s_nop 1
	v_cndmask_b32_e64 v10, v10, v15, s[0:1]
	v_mul_f32_e32 v12, 0x37800000, v10
	v_cndmask_b32_e32 v10, v10, v12, vcc
	v_cmp_class_f32_e32 vcc, v11, v13
	s_mov_b32 s0, 0x380637bd
	s_mov_b32 s1, 0x350637bd
	v_cndmask_b32_e32 v10, v10, v11, vcc
	v_mul_f32_e32 v7, v7, v10
	v_mul_f32_e32 v7, 0x3f800347, v7
	v_pk_mul_f32 v[8:9], v[8:9], s[0:1]
	s_nop 0
	v_fmamk_f32 v7, v7, 0x3888509c, v9
	v_add_f32_e32 v7, v8, v7
	v_add_f32_e32 v7, 0xda24260, v7
	v_add_f32_e32 v6, v6, v7
	v_cmp_le_f32_e64 s[8:9], v2, v6
	v_cmp_le_f32_e64 s[6:7], v3, v6
	v_cmp_le_f32_e64 s[4:5], v4, v6
	v_lshl_add_u64 v[2:3], s[22:23], 0, v[18:19]
	s_and_b32 s19, s8, 0xffff
	s_lshl_b32 s22, s6, 16
	v_cmp_le_f32_e64 s[0:1], v5, v6
	s_or_b32 s24, s19, s22
	s_and_b32 s23, s4, 0xffff
	s_mov_b32 s22, s25
	s_or_b64 s[22:23], s[24:25], s[22:23]
	s_lshl_b32 s27, s0, 16
	s_or_b64 s[26:27], s[22:23], s[26:27]
	s_add_u32 s22, s26, -1
	s_addc_u32 s23, s27, -1
	s_and_b64 s[22:23], s[26:27], s[22:23]
	s_cmp_eq_u64 s[22:23], 0
	v_readlane_b32 s22, v14, 0
	s_cbranch_scc0 .Lslowout_0
